# v121 + phase-start code prefetch: after each grid-barrier wait all 8 waves touch the next 32 KiB of code
# speedup vs baseline: 1.0068x; 1.0030x over previous
.LBB0_239:
	s_or_b64 exec, exec, s[0:1]
	s_barrier
	s_getpc_b64 s[100:101]
	v_mbcnt_lo_u32_b32 v250, -1, 0
	v_mbcnt_hi_u32_b32 v250, -1, v250
	v_lshlrev_b32_e32 v250, 6, v250
	v_mov_b32_e32 v251, s98
	v_lshl_add_u32 v250, v251, 12, v250
	global_load_dword v251, v250, s[100:101]

.LBB0_2396:
	s_or_b64 exec, exec, s[0:1]
	s_barrier
	s_getpc_b64 s[100:101]
	v_mbcnt_lo_u32_b32 v250, -1, 0
	v_mbcnt_hi_u32_b32 v250, -1, v250
	v_lshlrev_b32_e32 v250, 6, v250
	v_mov_b32_e32 v251, s98
	v_lshl_add_u32 v250, v251, 12, v250
	v_min_u32_e32 v250, 0x7f00, v250
	global_load_dword v251, v250, s[100:101]

.LBB0_2821:
	s_or_b64 exec, exec, s[0:1]
	s_barrier
	s_getpc_b64 s[100:101]
	v_mbcnt_lo_u32_b32 v250, -1, 0
	v_mbcnt_hi_u32_b32 v250, -1, v250
	v_lshlrev_b32_e32 v250, 6, v250
	v_mov_b32_e32 v251, s98
	v_lshl_add_u32 v250, v251, 12, v250
	v_min_u32_e32 v250, 0x2800, v250
	global_load_dword v251, v250, s[100:101]

	.amdhsa_kernel _Z4mega5MArgs
		.amdhsa_group_segment_fixed_size 0
		.amdhsa_private_segment_fixed_size 0
		.amdhsa_kernarg_size 496
		.amdhsa_user_sgpr_count 2
		.amdhsa_user_sgpr_dispatch_ptr 0
		.amdhsa_user_sgpr_queue_ptr 0
		.amdhsa_user_sgpr_kernarg_segment_ptr 1
		.amdhsa_user_sgpr_dispatch_id 0
		.amdhsa_user_sgpr_kernarg_preload_length 0
		.amdhsa_user_sgpr_kernarg_preload_offset 0
		.amdhsa_user_sgpr_private_segment_size 0
		.amdhsa_uses_dynamic_stack 0
		.amdhsa_enable_private_segment 0
		.amdhsa_system_sgpr_workgroup_id_x 1
		.amdhsa_system_sgpr_workgroup_id_y 0
		.amdhsa_system_sgpr_workgroup_id_z 0
		.amdhsa_system_sgpr_workgroup_info 0
		.amdhsa_system_vgpr_workitem_id 0
		.amdhsa_next_free_vgpr 252
		.amdhsa_next_free_sgpr 102
		.amdhsa_accum_offset 252
		.amdhsa_reserve_vcc 1
		.amdhsa_float_round_mode_32 0
		.amdhsa_float_round_mode_16_64 0
		.amdhsa_float_denorm_mode_32 3
		.amdhsa_float_denorm_mode_16_64 3
		.amdhsa_dx10_clamp 1
		.amdhsa_ieee_mode 1
		.amdhsa_fp16_overflow 0
		.amdhsa_tg_split 0
		.amdhsa_exception_fp_ieee_invalid_op 0
		.amdhsa_exception_fp_denorm_src 0
		.amdhsa_exception_fp_ieee_div_zero 0
		.amdhsa_exception_fp_ieee_overflow 0
		.amdhsa_exception_fp_ieee_underflow 0
		.amdhsa_exception_fp_ieee_inexact 0
		.amdhsa_exception_int_div_zero 0
	.end_amdhsa_kernel

amdhsa.kernels:
  - .agpr_count:     0
    .args:
      - .offset:         0
        .size:           240
        .value_kind:     by_value
      - .offset:         240
        .size:           4
        .value_kind:     hidden_block_count_x
      - .offset:         244
        .size:           4
        .value_kind:     hidden_block_count_y
      - .offset:         248
        .size:           4
        .value_kind:     hidden_block_count_z
      - .offset:         252
        .size:           2
        .value_kind:     hidden_group_size_x
      - .offset:         254
        .size:           2
        .value_kind:     hidden_group_size_y
      - .offset:         256
        .size:           2
        .value_kind:     hidden_group_size_z
      - .offset:         258
        .size:           2
        .value_kind:     hidden_remainder_x
      - .offset:         260
        .size:           2
        .value_kind:     hidden_remainder_y
      - .offset:         262
        .size:           2
        .value_kind:     hidden_remainder_z
      - .offset:         280
        .size:           8
        .value_kind:     hidden_global_offset_x
      - .offset:         288
        .size:           8
        .value_kind:     hidden_global_offset_y
      - .offset:         296
        .size:           8
        .value_kind:     hidden_global_offset_z
      - .offset:         304
        .size:           2
        .value_kind:     hidden_grid_dims
      - .offset:         360
        .size:           4
        .value_kind:     hidden_dynamic_lds_size
    .group_segment_fixed_size: 0
    .kernarg_segment_align: 8
    .kernarg_segment_size: 496
    .language:       OpenCL C
    .language_version:
      - 2
      - 0
    .max_flat_workgroup_size: 512
    .name:           _Z4mega5MArgs
    .private_segment_fixed_size: 0
    .sgpr_count:     108
    .sgpr_spill_count: 65
    .symbol:         _Z4mega5MArgs.kd
    .uniform_work_group_size: 1
    .uses_dynamic_stack: false
    .vgpr_count:     252
    .vgpr_spill_count: 0
    .wavefront_size: 64
